# P3: next unit's two parameter loads issued before the current unit's stores (no vmcnt(0) at the unit start)
# speedup vs baseline: 1.0093x; 1.0023x over previous
.LBB0_334:
	s_cmp_gt_i32 s78, 3
	s_cselect_b64 s[0:1], -1, 0
	s_cmp_lt_i32 s79, 4
	s_cselect_b64 s[4:5], -1, 0
	s_or_b64 s[0:1], s[0:1], s[4:5]
	s_or_b64 s[0:1], s[0:1], s[30:31]
	s_and_b64 vcc, exec, s[0:1]
	s_cbranch_vccnz .LBB0_394
	s_cmpk_gt_i32 s20, 0x7ff
	s_cbranch_scc1 .LBB0_344
	s_ashr_i32 s0, s20, 10
	s_add_u32 s12, s76, 0x364e8000
	s_addc_u32 s13, s77, 0
	s_ashr_i32 s1, s0, 31
	s_lshl_b32 s4, s20, 6
	s_waitcnt vmcnt(0)
	v_lshrrev_b32_e32 v21, 3, v0
	v_mov_b32_e32 v1, 0x1ff0
	s_lshl_b64 s[0:1], s[0:1], 13
	v_bitop3_b32 v1, s4, v1, v21 bitop3:0xc8
	v_or_b32_e32 v1, s0, v1
	s_movk_i32 s21, 0x3800
	v_mov_b64_e32 v[2:3], s[12:13]
	v_mad_u64_u32 v[4:5], s[4:5], v1, s21, v[2:3]
	v_mov_b32_e32 v1, 0x3800
	s_and_b32 s0, s20, 0x380
	v_and_b32_e32 v20, 0x7f, v0
	v_mad_i32_i24 v5, s1, v1, v5
	s_lshl_b32 s14, s0, 1
	s_mov_b32 s15, 0
	v_mov_b32_e32 v3, 0
	v_lshlrev_b32_e32 v2, 1, v20
	v_lshl_add_u64 v[4:5], v[4:5], 0, s[14:15]
	v_lshl_add_u64 v[4:5], v[4:5], 0, v[2:3]
	s_movk_i32 s25, 0x2000
	v_add_co_u32_e32 v6, vcc, s25, v4
	s_movk_i32 s30, 0x5000
	s_nop 0
	v_addc_co_u32_e32 v7, vcc, 0, v5, vcc
	v_add_co_u32_e32 v8, vcc, s30, v4
	s_mov_b32 s31, 0x9000
	s_nop 0
	v_addc_co_u32_e32 v9, vcc, 0, v5, vcc
	v_add_co_u32_e32 v10, vcc, s31, v4
	s_mov_b32 s34, 0xc000
	s_nop 0
	v_addc_co_u32_e32 v11, vcc, 0, v5, vcc
	v_add_co_u32_e32 v12, vcc, s34, v4
	s_mov_b32 s35, 0x10000
	s_nop 0
	v_addc_co_u32_e32 v13, vcc, 0, v5, vcc
	v_add_co_u32_e32 v14, vcc, s35, v4
	s_waitcnt lgkmcnt(0)
	s_mov_b32 s42, 0x17000
	v_addc_co_u32_e32 v15, vcc, 0, v5, vcc
	v_add_co_u32_e32 v16, vcc, s42, v4
	s_mov_b32 s43, 0x1e000
	s_nop 0
	v_addc_co_u32_e32 v17, vcc, 0, v5, vcc
	v_add_co_u32_e32 v18, vcc, s43, v4
	s_mov_b32 s48, 0x25000
	s_nop 0
	v_addc_co_u32_e32 v19, vcc, 0, v5, vcc
	v_add_co_u32_e32 v22, vcc, s48, v4
	s_mov_b32 s49, 0x2c000
	s_nop 0
	v_addc_co_u32_e32 v23, vcc, 0, v5, vcc
	v_add_co_u32_e32 v24, vcc, s49, v4
	s_mov_b32 s54, 0x33000
	s_nop 0
	v_addc_co_u32_e32 v25, vcc, 0, v5, vcc
	v_add_co_u32_e32 v26, vcc, s54, v4
	s_movk_i32 s55, 0x6000
	s_nop 0
	v_addc_co_u32_e32 v27, vcc, 0, v5, vcc
	v_add_co_u32_e32 v28, vcc, s55, v4
	s_mov_b32 s56, 0xd000
	s_nop 0
	v_addc_co_u32_e32 v29, vcc, 0, v5, vcc
	v_add_co_u32_e32 v30, vcc, s56, v4
	s_mov_b32 s57, 0x14000
	s_nop 0
	v_addc_co_u32_e32 v31, vcc, 0, v5, vcc
	v_add_co_u32_e32 v32, vcc, s57, v4
	s_mov_b32 s58, 0x1b000
	s_nop 0
	v_addc_co_u32_e32 v33, vcc, 0, v5, vcc
	v_add_co_u32_e32 v34, vcc, s58, v4
	s_mov_b32 s59, 0x22000
	s_nop 0
	v_addc_co_u32_e32 v35, vcc, 0, v5, vcc
	v_add_co_u32_e32 v36, vcc, s59, v4
	s_mov_b32 s60, 0x29000
	s_nop 0
	v_addc_co_u32_e32 v37, vcc, 0, v5, vcc
	v_add_co_u32_e32 v38, vcc, s60, v4
	s_mov_b32 s61, 0x30000
	s_nop 0
	v_addc_co_u32_e32 v39, vcc, 0, v5, vcc
	v_add_co_u32_e32 v40, vcc, s61, v4
	s_mov_b32 s64, 0x37000
	s_nop 0
	v_addc_co_u32_e32 v41, vcc, 0, v5, vcc
	v_add_co_u32_e32 v42, vcc, s64, v4
	s_mov_b32 s65, 0x13000
	s_nop 0
	v_addc_co_u32_e32 v43, vcc, 0, v5, vcc
	global_load_ushort v2, v[18:19], off offset:2048
	global_load_ushort v44, v[16:17], off offset:2048
	global_load_ushort v45, v[26:27], off offset:2048
	global_load_ushort v46, v[24:25], off offset:2048
	global_load_ushort v47, v[22:23], off offset:2048
	s_nop 0
	global_load_ushort v28, v[28:29], off
	s_nop 0
	global_load_ushort v29, v[30:31], off
	s_nop 0
	global_load_ushort v30, v[32:33], off
	global_load_ushort v31, v[34:35], off
	s_nop 0
	global_load_ushort v32, v[36:37], off
	global_load_ushort v33, v[38:39], off
	global_load_ushort v34, v[40:41], off
	global_load_ushort v35, v[42:43], off
	s_nop 0
	global_load_ushort v36, v[10:11], off
	global_load_ushort v37, v[14:15], off
	global_load_ushort v38, v[6:7], off offset:2048
	global_load_ushort v39, v[10:11], off offset:2048
	s_nop 0
	global_load_ushort v14, v[14:15], off offset:2048
	s_nop 0
	global_load_ushort v40, v[12:13], off offset:2048
	global_load_ushort v41, v[8:9], off offset:2048
	global_load_ushort v42, v[6:7], off
	v_add_co_u32_e32 v6, vcc, s65, v4
	s_mov_b32 s66, 0x1a000
	s_nop 0
	v_addc_co_u32_e32 v7, vcc, 0, v5, vcc
	v_add_co_u32_e32 v8, vcc, s66, v4
	s_mov_b32 s67, 0x21000
	s_nop 0
	v_addc_co_u32_e32 v9, vcc, 0, v5, vcc
	v_add_co_u32_e32 v10, vcc, s67, v4
	s_mov_b32 s68, 0x28000
	s_nop 0
	v_addc_co_u32_e32 v11, vcc, 0, v5, vcc
	global_load_ushort v48, v[18:19], off
	global_load_ushort v49, v[22:23], off
	s_nop 0
	global_load_ushort v11, v[10:11], off offset:2048
	s_nop 0
	global_load_ushort v50, v[8:9], off offset:2048
	global_load_ushort v51, v[6:7], off offset:2048
	global_load_ushort v52, v[16:17], off
	v_add_co_u32_e32 v6, vcc, s68, v4
	s_mov_b32 s69, 0x2f000
	s_nop 0
	v_addc_co_u32_e32 v7, vcc, 0, v5, vcc
	v_add_co_u32_e32 v8, vcc, s69, v4
	s_mov_b32 s70, 0x36000
	s_nop 0
	v_addc_co_u32_e32 v9, vcc, 0, v5, vcc
	v_add_co_u32_e32 v4, vcc, s70, v4
	s_movk_i32 s0, 0x7f
	s_nop 0
	v_addc_co_u32_e32 v5, vcc, 0, v5, vcc
	global_load_ushort v4, v[4:5], off offset:2048
	s_nop 0
	global_load_ushort v5, v[8:9], off offset:2048
	s_nop 0
	global_load_ushort v6, v[6:7], off offset:2048
	s_nop 0
	global_load_ushort v7, v[24:25], off
	global_load_ushort v8, v[26:27], off
	v_cmp_lt_u32_e64 s[4:5], s0, v0
	s_movk_i32 s0, 0xff
	v_cmp_lt_u32_e64 s[6:7], s0, v0
	s_movk_i32 s0, 0x17f
	v_cmp_lt_u32_e64 s[8:9], s0, v0
	s_movk_i32 s0, 0x1ff
	s_add_u32 s71, s76, 0x505e8000
	v_cmp_lt_u32_e64 s[10:11], s0, v0
	s_movk_i32 s0, 0x8c
	s_addc_u32 s72, s77, 0
	s_lshl_b32 s14, s91, 4
	v_and_b32_e32 v10, 48, v190
	s_movk_i32 s1, 0x80
	v_add_u32_e32 v10, 0, v10
	v_cmp_gt_u32_e32 vcc, s1, v0
	s_add_u32 s16, s76, 0x445e8000
	s_addc_u32 s17, s77, 0
	s_mov_b32 s73, 0x5040100
	v_and_b32_e32 v21, 48, v21
	s_sub_i32 s74, 0, s3
	s_lshl_b32 s18, s14, 1
	s_movk_i32 s82, 0x7000
	s_mov_b32 s83, s2
	s_waitcnt vmcnt(16)
	v_lshl_or_b32 v16, v28, 16, v38
	s_waitcnt vmcnt(15)
	v_lshl_or_b32 v17, v29, 16, v39
	v_lshl_or_b32 v12, v32, 16, v2
	v_lshrrev_b32_e32 v2, 2, v0
	s_waitcnt vmcnt(14)
	v_lshl_or_b32 v18, v30, 16, v14
	v_lshl_or_b32 v13, v33, 16, v47
	v_lshl_add_u32 v30, v20, 2, 0
	v_and_b32_e32 v33, 0x60, v2
	v_and_b32_e32 v2, 15, v0
	v_mad_u32_u24 v32, v20, s0, v30
	v_or_b32_e32 v9, s14, v2
	s_movk_i32 s0, 0x90
	v_lshl_or_b32 v19, v31, 16, v44
	v_mul_u32_u24_e32 v31, 0x90, v2
	v_lshlrev_b32_e32 v26, 7, v2
	v_lshrrev_b32_e32 v2, 2, v190
	v_and_b32_e32 v24, 12, v2
	v_mov_b32_e32 v2, v3
	s_waitcnt vmcnt(8)
	v_mad_u64_u32 v[22:23], s[0:1], v9, s0, v[10:11]
	s_lshl_b32 s0, s3, 1
	s_add_i32 s1, s2, s33
	s_sub_i32 s75, s33, s0
	s_sub_i32 s0, s1, s0
	v_mov_b32_e32 v9, v3
	v_perm_b32 v29, v11, v48, s73
	s_lshl_b32 s80, s0, 6
	s_lshl_b32 s0, s33, 6
	s_lshl_b32 s1, s3, 6
	v_add_u32_e32 v31, v10, v31
	v_lshl_or_b32 v14, v34, 16, v46
	v_lshl_or_b32 v15, v35, 16, v45
	v_perm_b32 v44, v41, v42, s73
	v_perm_b32 v43, v40, v36, s73
	s_waitcnt vmcnt(6)
	v_perm_b32 v42, v51, v37, s73
	s_waitcnt vmcnt(2)
	v_perm_b32 v28, v6, v49, s73
	s_waitcnt vmcnt(1)
	v_perm_b32 v27, v5, v7, s73
	s_waitcnt vmcnt(0)
	v_perm_b32 v25, v4, v8, s73
	v_mov_b32_e32 v4, v3
	v_mov_b32_e32 v5, v3
	v_mov_b32_e32 v6, v3
	v_mov_b32_e32 v7, v3
	v_mov_b32_e32 v8, v3
	v_mov_b64_e32 v[10:11], v[8:9]
	v_perm_b32 v41, v50, v52, s73
	s_sub_i32 s81, s0, s1
	v_lshlrev_b32_e32 v23, 2, v0
	v_lshlrev_b32_e32 v24, 1, v24
	v_lshlrev_b32_e32 v26, 1, v26
	v_add_u32_e32 v32, v32, v33
	v_mov_b64_e32 v[8:9], v[6:7]
	v_mov_b64_e32 v[6:7], v[4:5]
	v_mov_b64_e32 v[4:5], v[2:3]
	v_mov_b32_e32 v33, 0
	v_mov_b32_e32 v34, 0
	v_mov_b32_e32 v35, 0
	v_mov_b32_e32 v36, 0
	v_mov_b32_e32 v37, 0
	v_mov_b32_e32 v38, 0
	v_mov_b32_e32 v39, 0
	v_mov_b32_e32 v40, 0
	s_add_i32 s99, s74, s83
	s_and_b32 s99, s99, 0x380
	v_or_b32_e32 v153, s99, v20
	v_lshlrev_b32_e32 v153, 2, v153
	v_add_u32_e32 v154, 0x1000, v153
	global_load_dword v151, v153, s[38:39]
	global_load_dword v152, v154, s[38:39]
	s_waitcnt vmcnt(0)
	s_branch .LBB0_338
.LBB0_337:
	s_or_b64 exec, exec, s[22:23]
	ds_write_b128 v32, v[16:19] offset:18432
	ds_write_b128 v32, v[12:15] offset:18448
	s_waitcnt lgkmcnt(0)
	s_barrier
	ds_read_b128 v[12:15], v22
	ds_read_b128 v[16:19], v31 offset:18432
	ds_read_b128 v[42:45], v22 offset:64
	ds_read_b128 v[46:49], v31 offset:18496
	ds_read_b128 v[50:53], v31 offset:20736
	ds_read_b128 v[54:57], v31 offset:20800
	ds_read_b128 v[58:61], v31 offset:23040
	ds_read_b128 v[62:65], v31 offset:23104
	v_lshlrev_b64 v[28:29], 22, v[28:29]
	ds_read_b128 v[66:69], v31 offset:25344
	ds_read_b128 v[70:73], v31 offset:25408
	ds_read_b128 v[74:77], v31 offset:27648
	ds_read_b128 v[78:81], v31 offset:27712
	ds_read_b128 v[82:85], v31 offset:29952
	ds_read_b128 v[86:89], v31 offset:30016
	ds_read_b128 v[90:93], v31 offset:32256
	ds_read_b128 v[94:97], v31 offset:32320
	ds_read_b128 v[98:101], v31 offset:34560
	ds_read_b128 v[102:105], v31 offset:34624
	v_lshl_add_u64 v[28:29], s[16:17], 0, v[28:29]
	s_lshl_b32 s14, s14, 15
	s_waitcnt lgkmcnt(14)
	v_mfma_f32_16x16x32_bf16 v[16:19], v[12:15], v[16:19], 0
	v_lshl_add_u64 v[28:29], v[28:29], 0, s[14:15]
	s_mov_b32 s19, s15
	v_lshl_add_u64 v[28:29], v[28:29], 0, s[18:19]
	s_waitcnt lgkmcnt(13)
	v_mfma_f32_16x16x32_bf16 v[50:53], v[12:15], v[50:53], 0
	v_mov_b32_e32 v25, v3
	v_lshl_add_u64 v[28:29], v[28:29], 0, v[24:25]
	v_mov_b32_e32 v27, v3
	s_waitcnt lgkmcnt(11)
	v_mfma_f32_16x16x32_bf16 v[58:61], v[12:15], v[58:61], 0
	v_lshl_add_u64 v[28:29], v[28:29], 0, v[26:27]
	s_add_i32 s83, s83, s24
	s_add_i32 s99, s74, s83
	s_and_b32 s99, s99, 0x380
	v_or_b32_e32 v153, s99, v20
	v_lshlrev_b32_e32 v153, 2, v153
	v_add_u32_e32 v154, 0x1000, v153
	global_load_dword v151, v153, s[38:39]
	global_load_dword v152, v154, s[38:39]
	s_add_i32 s80, s80, s81
	s_waitcnt lgkmcnt(9)
	v_mfma_f32_16x16x32_bf16 v[66:69], v[12:15], v[66:69], 0
	s_waitcnt lgkmcnt(7)
	v_mfma_f32_16x16x32_bf16 v[74:77], v[12:15], v[74:77], 0
	s_waitcnt lgkmcnt(5)
	v_mfma_f32_16x16x32_bf16 v[82:85], v[12:15], v[82:85], 0
	s_waitcnt lgkmcnt(3)
	v_mfma_f32_16x16x32_bf16 v[90:93], v[12:15], v[90:93], 0
	s_waitcnt lgkmcnt(1)
	v_mfma_f32_16x16x32_bf16 v[12:15], v[12:15], v[98:101], 0
	v_mfma_f32_16x16x32_bf16 v[16:19], v[42:45], v[46:49], v[16:19]
	v_mfma_f32_16x16x32_bf16 v[46:49], v[42:45], v[54:57], v[50:53]
	v_mfma_f32_16x16x32_bf16 v[50:53], v[42:45], v[62:65], v[58:61]
	v_add_co_u32_e64 v62, s[0:1], s25, v28
	v_cvt_pk_bf16_f32 v58, v16, v17
	v_cvt_pk_bf16_f32 v59, v18, v19
	global_store_dwordx2 v[28:29], v[58:59], off
	s_nop 0
	v_addc_co_u32_e64 v63, s[0:1], 0, v29, s[0:1]
	v_cvt_pk_bf16_f32 v58, v46, v47
	v_cvt_pk_bf16_f32 v59, v48, v49
	s_movk_i32 s0, 0x4000
	v_mfma_f32_16x16x32_bf16 v[54:57], v[42:45], v[70:73], v[66:69]
	global_store_dwordx2 v[62:63], v[58:59], off offset:-4096
	v_cvt_pk_bf16_f32 v50, v50, v51
	v_cvt_pk_bf16_f32 v51, v52, v53
	v_mfma_f32_16x16x32_bf16 v[16:19], v[42:45], v[78:81], v[74:77]
	global_store_dwordx2 v[62:63], v[50:51], off
	v_cvt_pk_bf16_f32 v50, v54, v55
	v_cvt_pk_bf16_f32 v51, v56, v57
	v_mfma_f32_16x16x32_bf16 v[46:49], v[42:45], v[86:89], v[82:85]
	v_mfma_f32_16x16x32_bf16 v[58:61], v[42:45], v[94:97], v[90:93]
	s_waitcnt lgkmcnt(0)
	v_mfma_f32_16x16x32_bf16 v[12:15], v[42:45], v[102:105], v[12:15]
	v_add_co_u32_e64 v42, s[0:1], s0, v28
	s_nop 0
	v_addc_co_u32_e64 v43, s[0:1], 0, v29, s[0:1]
	global_store_dwordx2 v[42:43], v[50:51], off offset:-4096
	v_cvt_pk_bf16_f32 v16, v16, v17
	v_cvt_pk_bf16_f32 v17, v18, v19
	v_add_co_u32_e64 v18, s[0:1], s55, v28
	global_store_dwordx2 v[42:43], v[16:17], off
	v_cvt_pk_bf16_f32 v16, v46, v47
	v_cvt_pk_bf16_f32 v17, v48, v49
	s_nop 0
	v_addc_co_u32_e64 v19, s[0:1], 0, v29, s[0:1]
	global_store_dwordx2 v[18:19], v[16:17], off offset:-4096
	v_cvt_pk_bf16_f32 v16, v58, v59
	v_cvt_pk_bf16_f32 v17, v60, v61
	global_store_dwordx2 v[18:19], v[16:17], off
	v_cvt_pk_bf16_f32 v12, v12, v13
	v_cvt_pk_bf16_f32 v13, v14, v15
	v_add_co_u32_e64 v14, s[0:1], s82, v28
	s_nop 0
	v_addc_co_u32_e64 v15, s[0:1], 0, v29, s[0:1]
	s_add_i32 s0, s74, s83
	global_store_dwordx2 v[14:15], v[12:13], off
	s_cmpk_lt_i32 s0, 0x800
	s_waitcnt vmcnt(8)
	v_perm_b32 v33, v33, v128, s73
	v_perm_b32 v4, v4, v136, s73
	v_perm_b32 v34, v34, v129, s73
	v_perm_b32 v5, v5, v137, s73
	v_perm_b32 v35, v35, v130, s73
	v_perm_b32 v6, v6, v138, s73
	v_perm_b32 v36, v36, v131, s73
	v_perm_b32 v7, v7, v139, s73
	v_perm_b32 v37, v37, v132, s73
	v_perm_b32 v8, v8, v140, s73
	v_perm_b32 v38, v38, v133, s73
	v_perm_b32 v9, v9, v141, s73
	v_perm_b32 v39, v39, v134, s73
	v_perm_b32 v10, v10, v142, s73
	v_perm_b32 v40, v40, v135, s73
	v_perm_b32 v11, v11, v143, s73
	v_mov_b32_e32 v41, v36
	v_mov_b32_e32 v27, v39
	v_mov_b32_e32 v25, v40
	v_mov_b32_e32 v44, v33
	v_mov_b32_e32 v19, v7
	v_mov_b32_e32 v15, v11
	v_mov_b32_e32 v14, v10
	v_mov_b32_e32 v13, v9
	v_mov_b32_e32 v12, v8
	v_mov_b32_e32 v18, v6
	v_mov_b32_e32 v17, v5
	v_mov_b32_e32 v16, v4
	v_mov_b32_e32 v43, v34
	v_mov_b32_e32 v42, v35
	v_mov_b32_e32 v29, v37
	v_mov_b32_e32 v28, v38
	s_barrier
	s_cbranch_scc0 .LBB0_344
.LBB0_338:
.LBB0_340:
	s_add_i32 s14, s74, s83
	s_and_b32 s0, s14, 0x380
	v_or_b32_e32 v2, s0, v20
	v_lshlrev_b32_e32 v2, 2, v2
	v_lshl_add_u64 v[46:47], s[38:39], 0, v[2:3]
	s_movk_i32 s0, 0x1000
	v_add_co_u32_e64 v46, s[0:1], s0, v46
	v_lshlrev_b32_e32 v49, 16, v41
	s_nop 0
	v_addc_co_u32_e64 v47, s[0:1], 0, v47, s[0:1]
	v_mov_b32_e32 v2, v151
	s_nop 0
	v_mov_b32_e32 v45, v152
	v_lshlrev_b32_e32 v50, 16, v29
	v_lshlrev_b32_e32 v46, 16, v44
	v_mul_f32_e32 v49, 0xbfb8aa3b, v49
	v_mul_f32_e32 v50, 0xbfb8aa3b, v50
	v_and_b32_e32 v44, 0xffff0000, v44
	v_and_b32_e32 v29, 0xffff0000, v29
	v_mul_f32_e32 v46, 0xbfb8aa3b, v46
	v_exp_f32_e32 v49, v49
	v_exp_f32_e32 v50, v50
	v_lshlrev_b32_e32 v47, 16, v43
	v_lshlrev_b32_e32 v51, 16, v28
	v_and_b32_e32 v28, 0xffff0000, v28
	v_mul_f32_e32 v44, 0xbfb8aa3b, v44
	v_mul_f32_e32 v29, 0xbfb8aa3b, v29
	v_exp_f32_e32 v46, v46
	v_mul_f32_e32 v47, 0xbfb8aa3b, v47
	v_mul_f32_e32 v28, 0xbfb8aa3b, v28
	v_exp_f32_e32 v44, v44
	v_exp_f32_e32 v29, v29
	v_mul_f32_e32 v51, 0xbfb8aa3b, v51
	v_exp_f32_e32 v47, v47
	v_exp_f32_e32 v28, v28
	v_exp_f32_e32 v51, v51
	v_add_f32_e32 v49, 1.0, v49
	v_add_f32_e32 v50, 1.0, v50
	v_add_f32_e32 v46, 1.0, v46
	v_add_f32_e32 v44, 1.0, v44
	v_add_f32_e32 v29, 1.0, v29
	v_rcp_f32_e32 v46, v46
	v_add_f32_e32 v47, 1.0, v47
	v_add_f32_e32 v28, 1.0, v28
	v_rcp_f32_e32 v44, v44
	v_and_b32_e32 v43, 0xffff0000, v43
	v_add_f32_e32 v51, 1.0, v51
	v_rcp_f32_e32 v47, v47
	v_rcp_f32_e32 v28, v28
	v_lshlrev_b32_e32 v48, 16, v42
	v_and_b32_e32 v42, 0xffff0000, v42
	v_mul_f32_e32 v43, 0xbfb8aa3b, v43
	v_mul_f32_e32 v48, 0xbfb8aa3b, v48
	v_mul_f32_e32 v42, 0xbfb8aa3b, v42
	v_exp_f32_e32 v43, v43
	v_lshlrev_b32_e32 v52, 16, v27
	v_exp_f32_e32 v48, v48
	v_exp_f32_e32 v42, v42
	v_and_b32_e32 v41, 0xffff0000, v41
	v_mul_f32_e32 v52, 0xbfb8aa3b, v52
	v_mul_f32_e32 v41, 0xbfb8aa3b, v41
	v_exp_f32_e32 v52, v52
	v_exp_f32_e32 v41, v41
	v_add_f32_e32 v43, 1.0, v43
	v_add_f32_e32 v48, 1.0, v48
	v_add_f32_e32 v42, 1.0, v42
	v_rcp_f32_e32 v43, v43
	v_rcp_f32_e32 v48, v48
	v_rcp_f32_e32 v42, v42
	v_add_f32_e32 v41, 1.0, v41
	v_rcp_f32_e32 v41, v41
	v_and_b32_e32 v27, 0xffff0000, v27
	v_mul_f32_e32 v27, 0xbfb8aa3b, v27
	v_exp_f32_e32 v27, v27
	s_ashr_i32 s0, s14, 7
	v_add_f32_e32 v27, 1.0, v27
	v_rcp_f32_e32 v27, v27
	s_add_i32 s98, s75, s83
	s_cmpk_gt_i32 s98, 0x7ff
	s_cbranch_scc1 .Lp3pf_done
	s_ashr_i32 s100, s98, 10
	s_ashr_i32 s101, s100, 31
	s_and_b32 s99, s80, 0x1fc0
	s_lshl_b64 s[100:101], s[100:101], 13
	v_or_b32_e32 v146, s99, v21
	v_or_b32_e32 v146, s100, v146
	v_mov_b64_e32 v[144:145], s[12:13]
	s_and_b32 s98, s98, 0x380
	s_lshl_b32 s98, s98, 1
	s_addk_i32 s98, 0x2000
	s_mov_b32 s99, 0
	v_mad_u64_u32 v[144:145], s[86:87], v146, s21, v[144:145]
	v_lshlrev_b32_e32 v148, 1, v20
	v_mov_b32_e32 v149, 0
	v_mad_i32_i24 v145, s101, v1, v145
	v_lshl_add_u64 v[148:149], v[148:149], 0, s[98:99]
	s_movk_i32 s100, 0x3800
	s_mov_b32 s101, 0
	v_lshl_add_u64 v[144:145], v[144:145], 0, v[148:149]
	global_load_ushort v128, v[144:145], off
	global_load_ushort v136, v[144:145], off offset:2048
	v_lshl_add_u64 v[144:145], v[144:145], 0, s[100:101]
	global_load_ushort v33, v[144:145], off
	global_load_ushort v4, v[144:145], off offset:2048
	v_lshl_add_u64 v[144:145], v[144:145], 0, s[100:101]
	global_load_ushort v129, v[144:145], off
	global_load_ushort v137, v[144:145], off offset:2048
	v_lshl_add_u64 v[144:145], v[144:145], 0, s[100:101]
	global_load_ushort v34, v[144:145], off
	global_load_ushort v5, v[144:145], off offset:2048
	v_lshl_add_u64 v[144:145], v[144:145], 0, s[100:101]
	global_load_ushort v130, v[144:145], off
	global_load_ushort v138, v[144:145], off offset:2048
	v_lshl_add_u64 v[144:145], v[144:145], 0, s[100:101]
	global_load_ushort v35, v[144:145], off
	global_load_ushort v6, v[144:145], off offset:2048
	v_lshl_add_u64 v[144:145], v[144:145], 0, s[100:101]
	global_load_ushort v131, v[144:145], off
	global_load_ushort v139, v[144:145], off offset:2048
	v_lshl_add_u64 v[144:145], v[144:145], 0, s[100:101]
	global_load_ushort v36, v[144:145], off
	global_load_ushort v7, v[144:145], off offset:2048
	v_lshl_add_u64 v[144:145], v[144:145], 0, s[100:101]
	global_load_ushort v132, v[144:145], off
	global_load_ushort v140, v[144:145], off offset:2048
	v_lshl_add_u64 v[144:145], v[144:145], 0, s[100:101]
	global_load_ushort v37, v[144:145], off
	global_load_ushort v8, v[144:145], off offset:2048
	v_lshl_add_u64 v[144:145], v[144:145], 0, s[100:101]
	global_load_ushort v133, v[144:145], off
	global_load_ushort v141, v[144:145], off offset:2048
	v_lshl_add_u64 v[144:145], v[144:145], 0, s[100:101]
	global_load_ushort v38, v[144:145], off
	global_load_ushort v9, v[144:145], off offset:2048
	v_lshl_add_u64 v[144:145], v[144:145], 0, s[100:101]
	global_load_ushort v134, v[144:145], off
	global_load_ushort v142, v[144:145], off offset:2048
	v_lshl_add_u64 v[144:145], v[144:145], 0, s[100:101]
	global_load_ushort v39, v[144:145], off
	global_load_ushort v10, v[144:145], off offset:2048
	v_lshl_add_u64 v[144:145], v[144:145], 0, s[100:101]
	global_load_ushort v135, v[144:145], off
	global_load_ushort v143, v[144:145], off offset:2048
	v_lshl_add_u64 v[144:145], v[144:145], 0, s[100:101]
	global_load_ushort v40, v[144:145], off
	global_load_ushort v11, v[144:145], off offset:2048
